# baseline (speedup 1.0000x reference)
.LBB3_13:
	s_or_b64 exec, exec, s[4:5]
	v_mov_b32_e32 v172, 0
	v_ashrrev_i32_e32 v1, 2, v0
	v_and_b32_e32 v1, 0xffffffc0, v1
	v_add_u32_e32 v1, s8, v1
	v_lshrrev_b32_e32 v130, 2, v0
	v_and_or_b32 v156, v130, 12, v1
	v_ashrrev_i32_e32 v157, 31, v156
	v_lshl_add_u64 v[150:151], v[156:157], 2, s[2:3]
	v_lshrrev_b32_e32 v254, 8, v0
	v_bfe_u32 v255, v0, 4, 2
	v_lshlrev_b32_e32 v254, 8, v254
	v_lshl_add_u32 v254, v255, 4, v254
	v_add_u32_e32 v254, 0x20000, v254
	ds_read_b128 v[138:141], v254
	ds_read_b128 v[142:145], v254 offset:64
	v_and_b32_e32 v130, 15, v0
	v_and_b32_e32 v180, 1, v0
	v_lshrrev_b32_e32 v0, 1, v0
	v_and_b32_e32 v131, 0x60, v0
	s_movk_i32 s3, 0xff6e
	v_lshl_or_b32 v131, s33, 8, v131
	v_lshlrev_b32_e32 v0, 4, v180
	v_or_b32_e32 v181, v131, v130
	v_bitop3_b32 v158, v131, s3, v130 bitop3:0xc8
	v_or_b32_e32 v130, v0, v156
	v_or_b32_e32 v132, 1, v181
	v_or_b32_e32 v134, 16, v158
	v_or_b32_e32 v136, 17, v181
	v_ashrrev_i32_e32 v131, 31, v130
	v_ashrrev_i32_e32 v133, 31, v132
	v_ashrrev_i32_e32 v135, 31, v134
	v_ashrrev_i32_e32 v137, 31, v136
	v_lshl_add_u64 v[160:161], v[130:131], 2, s[0:1]
	v_lshlrev_b64 v[152:153], 12, v[132:133]
	v_lshlrev_b64 v[148:149], 12, v[134:135]
	v_lshlrev_b64 v[146:147], 12, v[136:137]
	ds_read_b128 v[130:133], v254 offset:128
	ds_read_b128 v[134:137], v254 offset:192
	ds_read_b128 v[184:187], v254 offset:576
	ds_read_b128 v[188:191], v254 offset:512
	ds_read_b128 v[192:195], v254 offset:640
	ds_read_b128 v[196:199], v254 offset:704
	s_mov_b32 s2, 0x34800000
	v_cmp_eq_u32_e32 vcc, 0, v180
	v_mov_b32_e32 v173, 0
	v_mov_b32_e32 v174, 0
	v_mov_b32_e32 v175, 0
	v_ashrrev_i32_e32 v159, 31, v158
	v_mov_b32_e32 v176, 0
	v_mov_b32_e32 v177, 0
	v_mov_b32_e32 v178, 0
	v_mov_b32_e32 v179, 0
	v_lshlrev_b64 v[154:155], 12, v[158:159]
	v_lshl_add_u64 v[162:163], v[160:161], 0, v[154:155]
	v_lshl_add_u64 v[164:165], v[160:161], 0, v[152:153]
	v_lshl_add_u64 v[166:167], v[160:161], 0, v[148:149]
	v_mov_b32_e32 v1, 0
	s_waitcnt vmcnt(0) lgkmcnt(0)
	v_fma_f32 v128, v128, s2, v140
	v_fma_f32 v129, v129, s2, v141
	v_fma_f32 v126, v126, s2, v138
	v_fma_f32 v127, v127, s2, v139
	v_fma_f32 v120, v120, s2, v144
	v_fma_f32 v121, v121, s2, v145
	v_fma_f32 v118, v118, s2, v142
	v_fma_f32 v119, v119, s2, v143
	v_fma_f32 v124, v124, s2, v140
	v_fma_f32 v125, v125, s2, v141
	v_fma_f32 v122, v122, s2, v138
	v_fma_f32 v123, v123, s2, v139
	v_fma_f32 v168, v116, s2, v144
	v_fma_f32 v169, v117, s2, v145
	v_fma_f32 v170, v114, s2, v142
	v_fma_f32 v171, v115, s2, v143
	v_cndmask_b32_e32 v114, v129, v121, vcc
	v_cndmask_b32_e32 v115, v128, v120, vcc
	v_cndmask_b32_e32 v116, v127, v119, vcc
	v_cndmask_b32_e32 v117, v126, v118, vcc
	v_cndmask_b32_e32 v159, v125, v169, vcc
	v_cndmask_b32_e32 v180, v124, v168, vcc
	v_cndmask_b32_e32 v182, v123, v171, vcc
	v_cndmask_b32_e32 v183, v122, v170, vcc
	v_mov_b32_dpp v172, v117 quad_perm:[1,0,3,2] row_mask:0xf bank_mask:0xf
	v_mov_b32_dpp v173, v116 quad_perm:[1,0,3,2] row_mask:0xf bank_mask:0xf
	v_mov_b32_dpp v174, v115 quad_perm:[1,0,3,2] row_mask:0xf bank_mask:0xf
	v_mov_b32_dpp v175, v114 quad_perm:[1,0,3,2] row_mask:0xf bank_mask:0xf
	v_mov_b32_dpp v176, v183 quad_perm:[1,0,3,2] row_mask:0xf bank_mask:0xf
	v_mov_b32_dpp v177, v182 quad_perm:[1,0,3,2] row_mask:0xf bank_mask:0xf
	v_mov_b32_dpp v178, v180 quad_perm:[1,0,3,2] row_mask:0xf bank_mask:0xf
	v_mov_b32_dpp v179, v159 quad_perm:[1,0,3,2] row_mask:0xf bank_mask:0xf
	v_cndmask_b32_e32 v117, v175, v129, vcc
	v_cndmask_b32_e32 v116, v174, v128, vcc
	v_cndmask_b32_e32 v115, v173, v127, vcc
	v_cndmask_b32_e32 v114, v172, v126, vcc
	v_cndmask_b32_e32 v119, v119, v173, vcc
	v_fma_f32 v110, v110, s2, v138
	v_fma_f32 v111, v111, s2, v139
	v_fma_f32 v106, v106, s2, v142
	v_fma_f32 v107, v107, s2, v143
	v_cndmask_b32_e32 v121, v121, v175, vcc
	v_cndmask_b32_e32 v120, v120, v174, vcc
	v_cndmask_b32_e32 v118, v118, v172, vcc
	v_cndmask_b32_e32 v125, v179, v125, vcc
	v_cndmask_b32_e32 v124, v178, v124, vcc
	v_cndmask_b32_e32 v123, v177, v123, vcc
	v_cndmask_b32_e32 v122, v176, v122, vcc
	v_cndmask_b32_e32 v129, v169, v179, vcc
	v_cndmask_b32_e32 v128, v168, v178, vcc
	v_cndmask_b32_e32 v127, v171, v177, vcc
	v_cndmask_b32_e32 v126, v170, v176, vcc
	global_store_dwordx4 v[162:163], v[114:117], off sc1
	global_store_dwordx4 v[164:165], v[118:121], off sc1
	global_store_dwordx4 v[166:167], v[122:125], off sc1
	v_lshl_add_u64 v[114:115], v[160:161], 0, v[146:147]
	v_fma_f32 v112, v112, s2, v140
	v_fma_f32 v113, v113, s2, v141
	v_fma_f32 v108, v108, s2, v144
	v_fma_f32 v109, v109, s2, v145
	v_cndmask_b32_e32 v116, v111, v107, vcc
	v_mov_b32_e32 v119, 0
	global_store_dwordx4 v[114:115], v[126:129], off sc1
	v_cndmask_b32_e32 v115, v112, v108, vcc
	v_cndmask_b32_e32 v117, v110, v106, vcc
	v_mov_b32_e32 v118, 0
	v_mov_b32_dpp v119, v116 quad_perm:[1,0,3,2] row_mask:0xf bank_mask:0xf
	v_mov_b32_e32 v116, 0
	v_cndmask_b32_e32 v114, v113, v109, vcc
	v_mov_b32_dpp v118, v117 quad_perm:[1,0,3,2] row_mask:0xf bank_mask:0xf
	v_mov_b32_dpp v116, v115 quad_perm:[1,0,3,2] row_mask:0xf bank_mask:0xf
	v_mov_b32_e32 v115, 0
	v_cndmask_b32_e32 v112, v116, v112, vcc
	v_cndmask_b32_e32 v116, v108, v116, vcc
	v_mov_b32_dpp v115, v114 quad_perm:[1,0,3,2] row_mask:0xf bank_mask:0xf
	v_cndmask_b32_e32 v114, v106, v118, vcc
	v_or_b32_e32 v106, 0x80, v158
	v_cndmask_b32_e32 v113, v115, v113, vcc
	v_cndmask_b32_e32 v117, v109, v115, vcc
	v_cndmask_b32_e32 v115, v107, v119, vcc
	v_ashrrev_i32_e32 v107, 31, v106
	v_lshlrev_b64 v[108:109], 12, v[106:107]
	v_cndmask_b32_e32 v111, v119, v111, vcc
	v_cndmask_b32_e32 v110, v118, v110, vcc
	v_lshl_add_u64 v[106:107], v[160:161], 0, v[108:109]
	global_store_dwordx4 v[106:107], v[110:113], off sc1
	v_or_b32_e32 v106, 0x81, v181
	v_ashrrev_i32_e32 v107, 31, v106
	v_lshlrev_b64 v[106:107], 12, v[106:107]
	v_lshl_add_u64 v[110:111], v[160:161], 0, v[106:107]
	v_fma_f32 v102, v102, s2, v138
	v_fma_f32 v103, v103, s2, v139
	v_fma_f32 v98, v98, s2, v142
	v_fma_f32 v99, v99, s2, v143
	global_store_dwordx4 v[110:111], v[114:117], off sc1
	v_fma_f32 v104, v104, s2, v140
	v_fma_f32 v105, v105, s2, v141
	v_fma_f32 v100, v100, s2, v144
	v_fma_f32 v101, v101, s2, v145
	v_cndmask_b32_e32 v112, v103, v99, vcc
	v_mov_b32_e32 v115, 0
	v_cndmask_b32_e32 v111, v104, v100, vcc
	v_cndmask_b32_e32 v113, v102, v98, vcc
	v_mov_b32_e32 v114, 0
	v_mov_b32_dpp v115, v112 quad_perm:[1,0,3,2] row_mask:0xf bank_mask:0xf
	v_mov_b32_e32 v112, 0
	v_cndmask_b32_e32 v110, v105, v101, vcc
	v_mov_b32_dpp v114, v113 quad_perm:[1,0,3,2] row_mask:0xf bank_mask:0xf
	v_mov_b32_dpp v112, v111 quad_perm:[1,0,3,2] row_mask:0xf bank_mask:0xf
	v_mov_b32_e32 v111, 0
	v_cndmask_b32_e32 v104, v112, v104, vcc
	v_cndmask_b32_e32 v112, v100, v112, vcc
	v_mov_b32_dpp v111, v110 quad_perm:[1,0,3,2] row_mask:0xf bank_mask:0xf
	v_cndmask_b32_e32 v110, v98, v114, vcc
	v_or_b32_e32 v98, 0x90, v158
	v_cndmask_b32_e32 v105, v111, v105, vcc
	v_cndmask_b32_e32 v113, v101, v111, vcc
	v_cndmask_b32_e32 v111, v99, v115, vcc
	v_ashrrev_i32_e32 v99, 31, v98
	v_lshlrev_b64 v[100:101], 12, v[98:99]
	v_cndmask_b32_e32 v103, v115, v103, vcc
	v_cndmask_b32_e32 v102, v114, v102, vcc
	v_lshl_add_u64 v[98:99], v[160:161], 0, v[100:101]
	global_store_dwordx4 v[98:99], v[102:105], off sc1
	v_or_b32_e32 v98, 0x91, v181
	v_ashrrev_i32_e32 v99, 31, v98
	v_lshlrev_b64 v[98:99], 12, v[98:99]
	v_lshl_add_u64 v[102:103], v[160:161], 0, v[98:99]
	global_store_dwordx4 v[102:103], v[110:113], off sc1
	v_fma_f32 v96, v96, s2, v132
	v_fma_f32 v97, v97, s2, v133
	v_fma_f32 v94, v94, s2, v130
	v_fma_f32 v95, v95, s2, v131
	v_fma_f32 v104, v92, s2, v136
	v_fma_f32 v105, v93, s2, v137
	v_fma_f32 v110, v90, s2, v134
	v_fma_f32 v111, v91, s2, v135
	v_lshl_add_u64 v[102:103], v[0:1], 0, v[156:157]
	v_cndmask_b32_e32 v90, v97, v105, vcc
	v_cndmask_b32_e32 v91, v96, v104, vcc
	v_cndmask_b32_e32 v92, v95, v111, vcc
	v_cndmask_b32_e32 v93, v94, v110, vcc
	v_mov_b32_e32 v112, v1
	v_mov_b32_e32 v113, v1
	v_mov_b32_e32 v114, v1
	v_mov_b32_e32 v115, v1
	v_lshl_add_u64 v[102:103], v[102:103], 2, s[0:1]
	v_mov_b32_dpp v112, v93 quad_perm:[1,0,3,2] row_mask:0xf bank_mask:0xf
	v_mov_b32_dpp v113, v92 quad_perm:[1,0,3,2] row_mask:0xf bank_mask:0xf
	v_mov_b32_dpp v114, v91 quad_perm:[1,0,3,2] row_mask:0xf bank_mask:0xf
	v_mov_b32_dpp v115, v90 quad_perm:[1,0,3,2] row_mask:0xf bank_mask:0xf
	v_cndmask_b32_e32 v93, v115, v97, vcc
	v_cndmask_b32_e32 v92, v114, v96, vcc
	v_cndmask_b32_e32 v91, v113, v95, vcc
	v_cndmask_b32_e32 v90, v112, v94, vcc
	v_cndmask_b32_e32 v97, v105, v115, vcc
	v_cndmask_b32_e32 v96, v104, v114, vcc
	v_lshl_add_u64 v[104:105], v[102:103], 0, v[154:155]
	v_cndmask_b32_e32 v95, v111, v113, vcc
	v_cndmask_b32_e32 v94, v110, v112, vcc
	global_store_dwordx4 v[104:105], v[90:93], off offset:128 sc1
	v_fma_f32 v104, v82, s2, v134
	v_fma_f32 v105, v83, s2, v135
	v_mov_b32_e32 v111, v1
	v_lshl_add_u64 v[90:91], v[102:103], 0, v[152:153]
	global_store_dwordx4 v[90:91], v[94:97], off offset:128 sc1
	v_fma_f32 v90, v88, s2, v132
	v_fma_f32 v91, v89, s2, v133
	v_mov_b32_e32 v112, v1
	v_fma_f32 v94, v86, s2, v130
	v_fma_f32 v95, v87, s2, v131
	v_fma_f32 v96, v84, s2, v136
	v_fma_f32 v97, v85, s2, v137
	v_cndmask_b32_e32 v82, v94, v104, vcc
	s_nop 0
	v_cndmask_b32_e32 v110, v95, v105, vcc
	v_mov_b32_dpp v111, v82 quad_perm:[1,0,3,2] row_mask:0xf bank_mask:0xf
	s_nop 0
	v_cndmask_b32_e32 v92, v91, v97, vcc
	v_cndmask_b32_e32 v93, v90, v96, vcc
	v_mov_b32_dpp v112, v110 quad_perm:[1,0,3,2] row_mask:0xf bank_mask:0xf
	v_mov_b32_e32 v110, v1
	v_mov_b32_e32 v113, v1
	v_fma_f32 v80, v80, s2, v132
	v_fma_f32 v81, v81, s2, v133
	v_mov_b32_dpp v110, v93 quad_perm:[1,0,3,2] row_mask:0xf bank_mask:0xf
	v_mov_b32_dpp v113, v92 quad_perm:[1,0,3,2] row_mask:0xf bank_mask:0xf
	v_cndmask_b32_e32 v93, v113, v91, vcc
	v_cndmask_b32_e32 v92, v110, v90, vcc
	v_cndmask_b32_e32 v91, v112, v95, vcc
	v_cndmask_b32_e32 v90, v111, v94, vcc
	v_cndmask_b32_e32 v95, v105, v112, vcc
	v_cndmask_b32_e32 v94, v104, v111, vcc
	v_lshl_add_u64 v[104:105], v[102:103], 0, v[148:149]
	v_cndmask_b32_e32 v97, v97, v113, vcc
	v_cndmask_b32_e32 v96, v96, v110, vcc
	global_store_dwordx4 v[104:105], v[90:93], off offset:128 sc1
	v_fma_f32 v78, v78, s2, v130
	v_fma_f32 v79, v79, s2, v131
	v_fma_f32 v72, v72, s2, v132
	v_fma_f32 v73, v73, s2, v133
	v_lshl_add_u64 v[90:91], v[102:103], 0, v[146:147]
	global_store_dwordx4 v[90:91], v[94:97], off offset:128 sc1
	v_fma_f32 v90, v76, s2, v136
	v_fma_f32 v91, v77, s2, v137
	v_fma_f32 v92, v74, s2, v134
	v_fma_f32 v93, v75, s2, v135
	v_cndmask_b32_e32 v74, v81, v91, vcc
	v_cndmask_b32_e32 v75, v80, v90, vcc
	v_cndmask_b32_e32 v76, v79, v93, vcc
	v_cndmask_b32_e32 v77, v78, v92, vcc
	v_mov_b32_e32 v94, v1
	v_mov_b32_e32 v95, v1
	v_mov_b32_e32 v96, v1
	v_mov_b32_e32 v97, v1
	v_mov_b32_dpp v94, v77 quad_perm:[1,0,3,2] row_mask:0xf bank_mask:0xf
	v_mov_b32_dpp v95, v76 quad_perm:[1,0,3,2] row_mask:0xf bank_mask:0xf
	v_mov_b32_dpp v96, v75 quad_perm:[1,0,3,2] row_mask:0xf bank_mask:0xf
	v_mov_b32_dpp v97, v74 quad_perm:[1,0,3,2] row_mask:0xf bank_mask:0xf
	v_cndmask_b32_e32 v77, v97, v81, vcc
	v_cndmask_b32_e32 v76, v96, v80, vcc
	v_cndmask_b32_e32 v75, v95, v79, vcc
	v_cndmask_b32_e32 v74, v94, v78, vcc
	v_cndmask_b32_e32 v81, v91, v97, vcc
	v_cndmask_b32_e32 v80, v90, v96, vcc
	v_lshl_add_u64 v[90:91], v[102:103], 0, v[108:109]
	v_cndmask_b32_e32 v79, v93, v95, vcc
	v_cndmask_b32_e32 v78, v92, v94, vcc
	global_store_dwordx4 v[90:91], v[74:77], off offset:128 sc1
	v_fma_f32 v70, v70, s2, v130
	v_fma_f32 v71, v71, s2, v131
	s_nop 0
	v_fma_f32 v64, v64, s2, v190
	v_fma_f32 v65, v65, s2, v191
	v_lshl_add_u64 v[74:75], v[102:103], 0, v[106:107]
	global_store_dwordx4 v[74:75], v[78:81], off offset:128 sc1
	v_fma_f32 v74, v68, s2, v136
	v_fma_f32 v75, v69, s2, v137
	v_fma_f32 v76, v66, s2, v134
	v_fma_f32 v77, v67, s2, v135
	v_cndmask_b32_e32 v66, v73, v75, vcc
	v_cndmask_b32_e32 v67, v72, v74, vcc
	v_cndmask_b32_e32 v68, v71, v77, vcc
	v_cndmask_b32_e32 v69, v70, v76, vcc
	v_mov_b32_e32 v78, v1
	v_mov_b32_e32 v79, v1
	v_mov_b32_e32 v80, v1
	v_mov_b32_e32 v81, v1
	v_mov_b32_dpp v78, v69 quad_perm:[1,0,3,2] row_mask:0xf bank_mask:0xf
	v_mov_b32_dpp v79, v68 quad_perm:[1,0,3,2] row_mask:0xf bank_mask:0xf
	v_mov_b32_dpp v80, v67 quad_perm:[1,0,3,2] row_mask:0xf bank_mask:0xf
	v_mov_b32_dpp v81, v66 quad_perm:[1,0,3,2] row_mask:0xf bank_mask:0xf
	v_cndmask_b32_e32 v69, v81, v73, vcc
	v_cndmask_b32_e32 v68, v80, v72, vcc
	v_cndmask_b32_e32 v67, v79, v71, vcc
	v_cndmask_b32_e32 v66, v78, v70, vcc
	v_cndmask_b32_e32 v73, v75, v81, vcc
	v_cndmask_b32_e32 v72, v74, v80, vcc
	v_lshl_add_u64 v[74:75], v[102:103], 0, v[100:101]
	v_cndmask_b32_e32 v71, v77, v79, vcc
	v_cndmask_b32_e32 v70, v76, v78, vcc
	global_store_dwordx4 v[74:75], v[66:69], off offset:128 sc1
	v_fma_f32 v62, v62, s2, v188
	v_fma_f32 v63, v63, s2, v189
	v_mov_b32_e32 v74, v1
	v_lshl_add_u64 v[66:67], v[102:103], 0, v[98:99]
	global_store_dwordx4 v[66:67], v[70:73], off offset:128 sc1
	v_add_u32_e32 v66, 0x80, v156
	v_or_b32_e32 v68, v0, v66
	v_fma_f32 v70, v60, s2, v186
	v_fma_f32 v71, v61, s2, v187
	v_fma_f32 v72, v58, s2, v184
	v_fma_f32 v73, v59, s2, v185
	v_ashrrev_i32_e32 v69, 31, v68
	v_cndmask_b32_e32 v58, v65, v71, vcc
	v_cndmask_b32_e32 v59, v64, v70, vcc
	v_cndmask_b32_e32 v60, v63, v73, vcc
	v_cndmask_b32_e32 v61, v62, v72, vcc
	v_mov_b32_e32 v67, v1
	v_mov_b32_e32 v75, v1
	v_mov_b32_e32 v76, v1
	v_lshl_add_u64 v[68:69], v[68:69], 2, s[0:1]
	v_mov_b32_dpp v67, v61 quad_perm:[1,0,3,2] row_mask:0xf bank_mask:0xf
	v_mov_b32_dpp v74, v60 quad_perm:[1,0,3,2] row_mask:0xf bank_mask:0xf
	v_mov_b32_dpp v75, v59 quad_perm:[1,0,3,2] row_mask:0xf bank_mask:0xf
	v_mov_b32_dpp v76, v58 quad_perm:[1,0,3,2] row_mask:0xf bank_mask:0xf
	v_cndmask_b32_e32 v61, v76, v65, vcc
	v_cndmask_b32_e32 v60, v75, v64, vcc
	v_cndmask_b32_e32 v59, v74, v63, vcc
	v_cndmask_b32_e32 v58, v67, v62, vcc
	v_cndmask_b32_e32 v65, v71, v76, vcc
	v_cndmask_b32_e32 v64, v70, v75, vcc
	v_lshl_add_u64 v[70:71], v[68:69], 0, v[154:155]
	v_cndmask_b32_e32 v63, v73, v74, vcc
	v_cndmask_b32_e32 v62, v72, v67, vcc
	global_store_dwordx4 v[70:71], v[58:61], off sc1
	v_fma_f32 v70, v50, s2, v184
	v_fma_f32 v71, v51, s2, v185
	v_mov_b32_e32 v72, v1
	v_lshl_add_u64 v[58:59], v[68:69], 0, v[152:153]
	global_store_dwordx4 v[58:59], v[62:65], off sc1
	v_fma_f32 v58, v56, s2, v190
	v_fma_f32 v59, v57, s2, v191
	v_mov_b32_e32 v73, v1
	v_fma_f32 v62, v54, s2, v188
	v_fma_f32 v63, v55, s2, v189
	v_fma_f32 v64, v52, s2, v186
	v_fma_f32 v65, v53, s2, v187
	v_cndmask_b32_e32 v54, v62, v70, vcc
	s_nop 0
	v_cndmask_b32_e32 v67, v63, v71, vcc
	v_mov_b32_dpp v72, v54 quad_perm:[1,0,3,2] row_mask:0xf bank_mask:0xf
	s_nop 0
	v_cndmask_b32_e32 v60, v59, v65, vcc
	v_cndmask_b32_e32 v61, v58, v64, vcc
	v_mov_b32_dpp v73, v67 quad_perm:[1,0,3,2] row_mask:0xf bank_mask:0xf
	v_mov_b32_e32 v67, v1
	v_mov_b32_e32 v74, v1
	v_fma_f32 v48, v48, s2, v190
	v_fma_f32 v49, v49, s2, v191
	v_mov_b32_dpp v67, v61 quad_perm:[1,0,3,2] row_mask:0xf bank_mask:0xf
	v_mov_b32_dpp v74, v60 quad_perm:[1,0,3,2] row_mask:0xf bank_mask:0xf
	v_cndmask_b32_e32 v61, v74, v59, vcc
	v_cndmask_b32_e32 v60, v67, v58, vcc
	v_cndmask_b32_e32 v59, v73, v63, vcc
	v_cndmask_b32_e32 v58, v72, v62, vcc
	v_cndmask_b32_e32 v63, v71, v73, vcc
	v_cndmask_b32_e32 v62, v70, v72, vcc
	v_lshl_add_u64 v[70:71], v[68:69], 0, v[148:149]
	v_cndmask_b32_e32 v65, v65, v74, vcc
	v_cndmask_b32_e32 v64, v64, v67, vcc
	global_store_dwordx4 v[70:71], v[58:61], off sc1
	v_fma_f32 v46, v46, s2, v188
	v_fma_f32 v47, v47, s2, v189
	v_fma_f32 v40, v40, s2, v190
	v_fma_f32 v41, v41, s2, v191
	v_lshl_add_u64 v[58:59], v[68:69], 0, v[146:147]
	global_store_dwordx4 v[58:59], v[62:65], off sc1
	v_fma_f32 v58, v44, s2, v186
	v_fma_f32 v59, v45, s2, v187
	v_fma_f32 v60, v42, s2, v184
	v_fma_f32 v61, v43, s2, v185
	v_cndmask_b32_e32 v42, v49, v59, vcc
	v_cndmask_b32_e32 v43, v48, v58, vcc
	v_cndmask_b32_e32 v44, v47, v61, vcc
	v_cndmask_b32_e32 v45, v46, v60, vcc
	v_mov_b32_e32 v62, v1
	v_mov_b32_e32 v63, v1
	v_mov_b32_e32 v64, v1
	v_mov_b32_e32 v65, v1
	v_mov_b32_dpp v62, v45 quad_perm:[1,0,3,2] row_mask:0xf bank_mask:0xf
	v_mov_b32_dpp v63, v44 quad_perm:[1,0,3,2] row_mask:0xf bank_mask:0xf
	v_mov_b32_dpp v64, v43 quad_perm:[1,0,3,2] row_mask:0xf bank_mask:0xf
	v_mov_b32_dpp v65, v42 quad_perm:[1,0,3,2] row_mask:0xf bank_mask:0xf
	v_cndmask_b32_e32 v45, v65, v49, vcc
	v_cndmask_b32_e32 v44, v64, v48, vcc
	v_cndmask_b32_e32 v43, v63, v47, vcc
	v_cndmask_b32_e32 v42, v62, v46, vcc
	v_cndmask_b32_e32 v49, v59, v65, vcc
	v_cndmask_b32_e32 v48, v58, v64, vcc
	v_lshl_add_u64 v[58:59], v[68:69], 0, v[108:109]
	v_cndmask_b32_e32 v47, v61, v63, vcc
	v_cndmask_b32_e32 v46, v60, v62, vcc
	global_store_dwordx4 v[58:59], v[42:45], off sc1
	v_fma_f32 v38, v38, s2, v188
	v_fma_f32 v39, v39, s2, v189
	v_ashrrev_i32_e32 v67, 31, v66
	v_lshl_add_u64 v[42:43], v[68:69], 0, v[106:107]
	global_store_dwordx4 v[42:43], v[46:49], off sc1
	v_fma_f32 v42, v32, s2, v186
	v_fma_f32 v43, v33, s2, v187
	v_fma_f32 v44, v30, s2, v184
	v_fma_f32 v45, v31, s2, v185
	v_cndmask_b32_e32 v30, v41, v43, vcc
	v_cndmask_b32_e32 v31, v40, v42, vcc
	v_cndmask_b32_e32 v32, v39, v45, vcc
	v_cndmask_b32_e32 v33, v38, v44, vcc
	v_mov_b32_e32 v46, v1
	v_mov_b32_e32 v47, v1
	v_mov_b32_e32 v48, v1
	v_mov_b32_e32 v49, v1
	v_mov_b32_dpp v46, v33 quad_perm:[1,0,3,2] row_mask:0xf bank_mask:0xf
	v_mov_b32_dpp v47, v32 quad_perm:[1,0,3,2] row_mask:0xf bank_mask:0xf
	v_mov_b32_dpp v48, v31 quad_perm:[1,0,3,2] row_mask:0xf bank_mask:0xf
	v_mov_b32_dpp v49, v30 quad_perm:[1,0,3,2] row_mask:0xf bank_mask:0xf
	v_cndmask_b32_e32 v33, v49, v41, vcc
	v_cndmask_b32_e32 v32, v48, v40, vcc
	v_cndmask_b32_e32 v31, v47, v39, vcc
	v_cndmask_b32_e32 v30, v46, v38, vcc
	v_cndmask_b32_e32 v41, v43, v49, vcc
	v_cndmask_b32_e32 v40, v42, v48, vcc
	v_lshl_add_u64 v[42:43], v[68:69], 0, v[100:101]
	v_cndmask_b32_e32 v39, v45, v47, vcc
	v_cndmask_b32_e32 v38, v44, v46, vcc
	global_store_dwordx4 v[42:43], v[30:33], off sc1
	v_mov_b32_e32 v42, v1
	v_mov_b32_e32 v43, v1
	v_lshl_add_u64 v[30:31], v[68:69], 0, v[98:99]
	global_store_dwordx4 v[30:31], v[38:41], off sc1
	v_lshl_add_u64 v[30:31], v[0:1], 0, v[66:67]
	s_nop 0
	v_fma_f32 v32, v34, s2, v192
	v_fma_f32 v33, v35, s2, v193
	v_lshl_add_u64 v[38:39], v[30:31], 2, s[0:1]
	v_fma_f32 v30, v36, s2, v194
	v_fma_f32 v31, v37, s2, v195
	v_fma_f32 v34, v28, s2, v198
	v_fma_f32 v35, v29, s2, v199
	v_fma_f32 v36, v26, s2, v196
	v_fma_f32 v37, v27, s2, v197
	v_cndmask_b32_e32 v0, v31, v35, vcc
	v_cndmask_b32_e32 v26, v30, v34, vcc
	v_cndmask_b32_e32 v27, v33, v37, vcc
	v_cndmask_b32_e32 v28, v32, v36, vcc
	v_mov_b32_e32 v40, v1
	v_mov_b32_e32 v41, v1
	v_mov_b32_dpp v42, v26 quad_perm:[1,0,3,2] row_mask:0xf bank_mask:0xf
	v_mov_b32_dpp v40, v28 quad_perm:[1,0,3,2] row_mask:0xf bank_mask:0xf
	v_mov_b32_dpp v41, v27 quad_perm:[1,0,3,2] row_mask:0xf bank_mask:0xf
	v_mov_b32_dpp v43, v0 quad_perm:[1,0,3,2] row_mask:0xf bank_mask:0xf
	v_cndmask_b32_e32 v29, v43, v31, vcc
	v_cndmask_b32_e32 v28, v42, v30, vcc
	v_cndmask_b32_e32 v27, v41, v33, vcc
	v_cndmask_b32_e32 v26, v40, v32, vcc
	v_cndmask_b32_e32 v33, v35, v43, vcc
	v_cndmask_b32_e32 v32, v34, v42, vcc
	v_lshl_add_u64 v[34:35], v[38:39], 0, v[154:155]
	v_cndmask_b32_e32 v31, v37, v41, vcc
	v_cndmask_b32_e32 v30, v36, v40, vcc
	global_store_dwordx4 v[34:35], v[26:29], off offset:128 sc1
	v_fma_f32 v24, v24, s2, v194
	v_fma_f32 v25, v25, s2, v195
	v_fma_f32 v22, v22, s2, v192
	v_fma_f32 v23, v23, s2, v193
	v_lshl_add_u64 v[26:27], v[38:39], 0, v[152:153]
	global_store_dwordx4 v[26:27], v[30:33], off offset:128 sc1
	v_fma_f32 v26, v20, s2, v198
	v_fma_f32 v27, v21, s2, v199
	v_fma_f32 v28, v18, s2, v196
	v_fma_f32 v29, v19, s2, v197
	v_cndmask_b32_e32 v0, v25, v27, vcc
	v_cndmask_b32_e32 v18, v24, v26, vcc
	v_cndmask_b32_e32 v19, v23, v29, vcc
	v_cndmask_b32_e32 v20, v22, v28, vcc
	v_mov_b32_e32 v30, v1
	v_mov_b32_e32 v31, v1
	v_mov_b32_e32 v32, v1
	v_mov_b32_e32 v33, v1
	v_mov_b32_dpp v30, v20 quad_perm:[1,0,3,2] row_mask:0xf bank_mask:0xf
	v_mov_b32_dpp v31, v19 quad_perm:[1,0,3,2] row_mask:0xf bank_mask:0xf
	v_mov_b32_dpp v32, v18 quad_perm:[1,0,3,2] row_mask:0xf bank_mask:0xf
	v_mov_b32_dpp v33, v0 quad_perm:[1,0,3,2] row_mask:0xf bank_mask:0xf
	v_cndmask_b32_e32 v21, v33, v25, vcc
	v_cndmask_b32_e32 v20, v32, v24, vcc
	v_cndmask_b32_e32 v19, v31, v23, vcc
	v_cndmask_b32_e32 v18, v30, v22, vcc
	v_cndmask_b32_e32 v25, v27, v33, vcc
	v_cndmask_b32_e32 v24, v26, v32, vcc
	v_lshl_add_u64 v[26:27], v[38:39], 0, v[148:149]
	v_cndmask_b32_e32 v23, v29, v31, vcc
	v_cndmask_b32_e32 v22, v28, v30, vcc
	global_store_dwordx4 v[26:27], v[18:21], off offset:128 sc1
	v_fma_f32 v16, v16, s2, v194
	v_fma_f32 v17, v17, s2, v195
	v_fma_f32 v14, v14, s2, v192
	v_fma_f32 v15, v15, s2, v193
	v_lshl_add_u64 v[18:19], v[38:39], 0, v[146:147]
	global_store_dwordx4 v[18:19], v[22:25], off offset:128 sc1
	v_fma_f32 v18, v12, s2, v198
	v_fma_f32 v19, v13, s2, v199
	v_fma_f32 v20, v10, s2, v196
	v_fma_f32 v21, v11, s2, v197
	v_cndmask_b32_e32 v0, v17, v19, vcc
	v_cndmask_b32_e32 v10, v16, v18, vcc
	v_cndmask_b32_e32 v11, v15, v21, vcc
	v_cndmask_b32_e32 v12, v14, v20, vcc
	v_mov_b32_e32 v22, v1
	v_mov_b32_e32 v23, v1
	v_mov_b32_e32 v24, v1
	v_mov_b32_e32 v25, v1
	v_mov_b32_dpp v22, v12 quad_perm:[1,0,3,2] row_mask:0xf bank_mask:0xf
	v_mov_b32_dpp v23, v11 quad_perm:[1,0,3,2] row_mask:0xf bank_mask:0xf
	v_mov_b32_dpp v24, v10 quad_perm:[1,0,3,2] row_mask:0xf bank_mask:0xf
	v_mov_b32_dpp v25, v0 quad_perm:[1,0,3,2] row_mask:0xf bank_mask:0xf
	v_cndmask_b32_e32 v13, v25, v17, vcc
	v_cndmask_b32_e32 v12, v24, v16, vcc
	v_cndmask_b32_e32 v11, v23, v15, vcc
	v_cndmask_b32_e32 v10, v22, v14, vcc
	v_cndmask_b32_e32 v17, v19, v25, vcc
	v_cndmask_b32_e32 v16, v18, v24, vcc
	v_lshl_add_u64 v[18:19], v[38:39], 0, v[108:109]
	v_cndmask_b32_e32 v15, v21, v23, vcc
	v_cndmask_b32_e32 v14, v20, v22, vcc
	global_store_dwordx4 v[18:19], v[10:13], off offset:128 sc1
	v_fma_f32 v8, v8, s2, v194
	v_fma_f32 v9, v9, s2, v195
	v_fma_f32 v6, v6, s2, v192
	v_fma_f32 v7, v7, s2, v193
	v_lshl_add_u64 v[10:11], v[38:39], 0, v[106:107]
	global_store_dwordx4 v[10:11], v[14:17], off offset:128 sc1
	v_fma_f32 v10, v4, s2, v198
	v_fma_f32 v11, v5, s2, v199
	v_fma_f32 v12, v2, s2, v196
	v_fma_f32 v13, v3, s2, v197
	v_cndmask_b32_e32 v0, v9, v11, vcc
	v_cndmask_b32_e32 v2, v8, v10, vcc
	v_cndmask_b32_e32 v3, v7, v13, vcc
	v_cndmask_b32_e32 v4, v6, v12, vcc
	v_mov_b32_e32 v14, v1
	v_mov_b32_e32 v15, v1
	v_mov_b32_e32 v16, v1
	v_mov_b32_dpp v14, v4 quad_perm:[1,0,3,2] row_mask:0xf bank_mask:0xf
	v_mov_b32_dpp v15, v3 quad_perm:[1,0,3,2] row_mask:0xf bank_mask:0xf
	v_mov_b32_dpp v16, v2 quad_perm:[1,0,3,2] row_mask:0xf bank_mask:0xf
	v_mov_b32_dpp v1, v0 quad_perm:[1,0,3,2] row_mask:0xf bank_mask:0xf
	v_cndmask_b32_e32 v5, v1, v9, vcc
	v_cndmask_b32_e32 v4, v16, v8, vcc
	v_cndmask_b32_e32 v3, v15, v7, vcc
	v_cndmask_b32_e32 v2, v14, v6, vcc
	v_cndmask_b32_e32 v9, v11, v1, vcc
	v_lshl_add_u64 v[0:1], v[38:39], 0, v[100:101]
	v_cndmask_b32_e32 v8, v10, v16, vcc
	v_cndmask_b32_e32 v7, v13, v15, vcc
	v_cndmask_b32_e32 v6, v12, v14, vcc
	global_store_dwordx4 v[0:1], v[2:5], off offset:128 sc1
	v_lshl_add_u64 v[0:1], v[38:39], 0, v[98:99]
	global_store_dwordx4 v[0:1], v[6:9], off offset:128 sc1
	s_endpgm
